# top-256 fast path with chunk-count granularity of 4 (7 loop variants per token) + P11 tile read batching
# speedup vs baseline: 1.0054x; 1.0021x over previous
.LBB0_1617:
	s_lshl_b64 s[0:1], s[0:1], 8
	v_readlane_b32 s4, v253, 13
	s_waitcnt lgkmcnt(0)
	v_readlane_b32 s5, v253, 14
	s_add_u32 s0, s4, s0
	s_barrier
	s_addc_u32 s1, s5, s1
	v_writelane_b32 v252, s0, 49
	s_and_b64 vcc, exec, s[26:27]
	v_writelane_b32 v254, s26, 35
	v_writelane_b32 v252, s1, 50
	s_nop 0
	v_writelane_b32 v254, s27, 36
	s_cmp_lt_u32 s33, 4
	s_cbranch_scc1 .Ltk0_orig
	s_mov_b32 s4, 0
	s_mov_b32 s5, 0x80000000
	s_cmp_lt_u32 s33, 8
	s_cbranch_scc1 .Ltk0_l8
	s_cmp_lt_u32 s33, 12
	s_cbranch_scc1 .Ltk0_l12
	s_cmp_lt_u32 s33, 16
	s_cbranch_scc1 .Ltk0_l16
	s_cmp_lt_u32 s33, 20
	s_cbranch_scc1 .Ltk0_l20
	s_cmp_lt_u32 s33, 24
	s_cbranch_scc1 .Ltk0_l24
	s_cmp_lt_u32 s33, 28
	s_cbranch_scc1 .Ltk0_l28

.Ltk0_l28:
	s_or_b32 s6, s4, s5
	v_cmp_le_u32_e64 s[8:9], s6, v172
	v_cmp_le_u32_e64 s[12:13], s6, v179
	v_cmp_le_u32_e64 s[16:17], s6, v181
	v_cndmask_b32_e64 v8, 0, 1, s[8:9]
	v_cmp_le_u32_e64 s[8:9], s6, v183
	v_addc_co_u32_e64 v8, s[20:21], 0, v8, s[12:13]
	v_cmp_le_u32_e64 s[12:13], s6, v185
	v_addc_co_u32_e64 v8, s[20:21], 0, v8, s[16:17]
	v_cmp_le_u32_e64 s[16:17], s6, v187
	v_addc_co_u32_e64 v8, s[20:21], 0, v8, s[8:9]
	v_cmp_le_u32_e64 s[8:9], s6, v189
	v_addc_co_u32_e64 v8, s[20:21], 0, v8, s[12:13]
	v_cmp_le_u32_e64 s[12:13], s6, v190
	v_addc_co_u32_e64 v8, s[20:21], 0, v8, s[16:17]
	v_cmp_le_u32_e64 s[16:17], s6, v191
	v_addc_co_u32_e64 v8, s[20:21], 0, v8, s[8:9]
	v_cmp_le_u32_e64 s[8:9], s6, v192
	v_addc_co_u32_e64 v8, s[20:21], 0, v8, s[12:13]
	v_cmp_le_u32_e64 s[12:13], s6, v193
	v_addc_co_u32_e64 v8, s[20:21], 0, v8, s[16:17]
	v_cmp_le_u32_e64 s[16:17], s6, v194
	v_addc_co_u32_e64 v8, s[20:21], 0, v8, s[8:9]
	v_cmp_le_u32_e64 s[8:9], s6, v195
	v_addc_co_u32_e64 v8, s[20:21], 0, v8, s[12:13]
	v_cmp_le_u32_e64 s[12:13], s6, v196
	v_addc_co_u32_e64 v8, s[20:21], 0, v8, s[16:17]
	v_cmp_le_u32_e64 s[16:17], s6, v198
	v_addc_co_u32_e64 v8, s[20:21], 0, v8, s[8:9]
	v_cmp_le_u32_e64 s[8:9], s6, v200
	v_addc_co_u32_e64 v8, s[20:21], 0, v8, s[12:13]
	v_cmp_le_u32_e64 s[12:13], s6, v206
	v_addc_co_u32_e64 v8, s[20:21], 0, v8, s[16:17]
	v_cmp_le_u32_e64 s[16:17], s6, v207
	v_addc_co_u32_e64 v8, s[20:21], 0, v8, s[8:9]
	v_cmp_le_u32_e64 s[8:9], s6, v208
	v_addc_co_u32_e64 v8, s[20:21], 0, v8, s[12:13]
	v_cmp_le_u32_e64 s[12:13], s6, v209
	v_addc_co_u32_e64 v8, s[20:21], 0, v8, s[16:17]
	v_cmp_le_u32_e64 s[16:17], s6, v210
	v_addc_co_u32_e64 v8, s[20:21], 0, v8, s[8:9]
	v_cmp_le_u32_e64 s[8:9], s6, v211
	v_addc_co_u32_e64 v8, s[20:21], 0, v8, s[12:13]
	v_cmp_le_u32_e64 s[12:13], s6, v212
	v_addc_co_u32_e64 v8, s[20:21], 0, v8, s[16:17]
	v_cmp_le_u32_e64 s[16:17], s6, v213
	v_addc_co_u32_e64 v8, s[20:21], 0, v8, s[8:9]
	v_cmp_le_u32_e64 s[8:9], s6, v214
	v_addc_co_u32_e64 v8, s[20:21], 0, v8, s[12:13]
	v_cmp_le_u32_e64 s[12:13], s6, v215
	v_addc_co_u32_e64 v8, s[20:21], 0, v8, s[16:17]
	v_cmp_le_u32_e64 s[16:17], s6, v216
	v_addc_co_u32_e64 v8, s[20:21], 0, v8, s[8:9]
	v_cmp_le_u32_e64 s[8:9], s6, v217
	v_addc_co_u32_e64 v8, s[20:21], 0, v8, s[12:13]
	v_addc_co_u32_e64 v8, s[20:21], 0, v8, s[16:17]
	v_addc_co_u32_e64 v8, s[20:21], 0, v8, s[8:9]
	v_and_b32_e32 v9, 16, v8
	v_cmp_ne_u32_e64 s[22:23], 0, v9
	v_and_b32_e32 v9, 8, v8
	v_cmp_ne_u32_e64 s[18:19], 0, v9
	v_and_b32_e32 v9, 4, v8
	v_cmp_ne_u32_e64 s[16:17], 0, v9
	v_and_b32_e32 v9, 2, v8
	v_cmp_ne_u32_e64 s[12:13], 0, v9
	v_and_b32_e32 v9, 1, v8
	v_cmp_ne_u32_e64 s[8:9], 0, v9
	s_bcnt1_i32_b64 s7, s[22:23]
	s_bcnt1_i32_b64 s3, s[18:19]
	s_lshl1_add_u32 s7, s7, s3
	s_bcnt1_i32_b64 s3, s[16:17]
	s_lshl1_add_u32 s7, s7, s3
	s_bcnt1_i32_b64 s3, s[12:13]
	s_lshl1_add_u32 s7, s7, s3
	s_bcnt1_i32_b64 s3, s[8:9]
	s_lshl1_add_u32 s7, s7, s3
	s_cmpk_lt_u32 s7, 0x100
	s_cselect_b32 s4, s4, s6
	s_cmpk_eq_u32 s7, 0x100
	s_cbranch_scc1 .Ltk0_x28
	s_lshr_b32 s5, s5, 1
	s_cbranch_scc1 .Ltk0_l28
	s_branch .Ltk0_orig

.Ltk0_l20:
	s_or_b32 s6, s4, s5
	v_cmp_le_u32_e64 s[8:9], s6, v172
	v_cmp_le_u32_e64 s[12:13], s6, v179
	v_cmp_le_u32_e64 s[16:17], s6, v181
	v_cndmask_b32_e64 v8, 0, 1, s[8:9]
	v_cmp_le_u32_e64 s[8:9], s6, v183
	v_addc_co_u32_e64 v8, s[20:21], 0, v8, s[12:13]
	v_cmp_le_u32_e64 s[12:13], s6, v185
	v_addc_co_u32_e64 v8, s[20:21], 0, v8, s[16:17]
	v_cmp_le_u32_e64 s[16:17], s6, v187
	v_addc_co_u32_e64 v8, s[20:21], 0, v8, s[8:9]
	v_cmp_le_u32_e64 s[8:9], s6, v189
	v_addc_co_u32_e64 v8, s[20:21], 0, v8, s[12:13]
	v_cmp_le_u32_e64 s[12:13], s6, v190
	v_addc_co_u32_e64 v8, s[20:21], 0, v8, s[16:17]
	v_cmp_le_u32_e64 s[16:17], s6, v191
	v_addc_co_u32_e64 v8, s[20:21], 0, v8, s[8:9]
	v_cmp_le_u32_e64 s[8:9], s6, v192
	v_addc_co_u32_e64 v8, s[20:21], 0, v8, s[12:13]
	v_cmp_le_u32_e64 s[12:13], s6, v193
	v_addc_co_u32_e64 v8, s[20:21], 0, v8, s[16:17]
	v_cmp_le_u32_e64 s[16:17], s6, v194
	v_addc_co_u32_e64 v8, s[20:21], 0, v8, s[8:9]
	v_cmp_le_u32_e64 s[8:9], s6, v195
	v_addc_co_u32_e64 v8, s[20:21], 0, v8, s[12:13]
	v_cmp_le_u32_e64 s[12:13], s6, v196
	v_addc_co_u32_e64 v8, s[20:21], 0, v8, s[16:17]
	v_cmp_le_u32_e64 s[16:17], s6, v198
	v_addc_co_u32_e64 v8, s[20:21], 0, v8, s[8:9]
	v_cmp_le_u32_e64 s[8:9], s6, v200
	v_addc_co_u32_e64 v8, s[20:21], 0, v8, s[12:13]
	v_cmp_le_u32_e64 s[12:13], s6, v206
	v_addc_co_u32_e64 v8, s[20:21], 0, v8, s[16:17]
	v_cmp_le_u32_e64 s[16:17], s6, v207
	v_addc_co_u32_e64 v8, s[20:21], 0, v8, s[8:9]
	v_cmp_le_u32_e64 s[8:9], s6, v208
	v_addc_co_u32_e64 v8, s[20:21], 0, v8, s[12:13]
	v_cmp_le_u32_e64 s[12:13], s6, v209
	v_addc_co_u32_e64 v8, s[20:21], 0, v8, s[16:17]
	v_addc_co_u32_e64 v8, s[20:21], 0, v8, s[8:9]
	v_addc_co_u32_e64 v8, s[20:21], 0, v8, s[12:13]
	v_and_b32_e32 v9, 16, v8
	v_cmp_ne_u32_e64 s[22:23], 0, v9
	v_and_b32_e32 v9, 8, v8
	v_cmp_ne_u32_e64 s[18:19], 0, v9
	v_and_b32_e32 v9, 4, v8
	v_cmp_ne_u32_e64 s[16:17], 0, v9
	v_and_b32_e32 v9, 2, v8
	v_cmp_ne_u32_e64 s[12:13], 0, v9
	v_and_b32_e32 v9, 1, v8
	v_cmp_ne_u32_e64 s[8:9], 0, v9
	s_bcnt1_i32_b64 s7, s[22:23]
	s_bcnt1_i32_b64 s3, s[18:19]
	s_lshl1_add_u32 s7, s7, s3
	s_bcnt1_i32_b64 s3, s[16:17]
	s_lshl1_add_u32 s7, s7, s3
	s_bcnt1_i32_b64 s3, s[12:13]
	s_lshl1_add_u32 s7, s7, s3
	s_bcnt1_i32_b64 s3, s[8:9]
	s_lshl1_add_u32 s7, s7, s3
	s_cmpk_lt_u32 s7, 0x100
	s_cselect_b32 s4, s4, s6
	s_cmpk_eq_u32 s7, 0x100
	s_cbranch_scc1 .Ltk0_x20
	s_lshr_b32 s5, s5, 1
	s_cbranch_scc1 .Ltk0_l20
	s_branch .Ltk0_orig

.Ltk0_l12:
	s_or_b32 s6, s4, s5
	v_cmp_le_u32_e64 s[8:9], s6, v172
	v_cmp_le_u32_e64 s[12:13], s6, v179
	v_cmp_le_u32_e64 s[16:17], s6, v181
	v_cndmask_b32_e64 v8, 0, 1, s[8:9]
	v_cmp_le_u32_e64 s[8:9], s6, v183
	v_addc_co_u32_e64 v8, s[20:21], 0, v8, s[12:13]
	v_cmp_le_u32_e64 s[12:13], s6, v185
	v_addc_co_u32_e64 v8, s[20:21], 0, v8, s[16:17]
	v_cmp_le_u32_e64 s[16:17], s6, v187
	v_addc_co_u32_e64 v8, s[20:21], 0, v8, s[8:9]
	v_cmp_le_u32_e64 s[8:9], s6, v189
	v_addc_co_u32_e64 v8, s[20:21], 0, v8, s[12:13]
	v_cmp_le_u32_e64 s[12:13], s6, v190
	v_addc_co_u32_e64 v8, s[20:21], 0, v8, s[16:17]
	v_cmp_le_u32_e64 s[16:17], s6, v191
	v_addc_co_u32_e64 v8, s[20:21], 0, v8, s[8:9]
	v_cmp_le_u32_e64 s[8:9], s6, v192
	v_addc_co_u32_e64 v8, s[20:21], 0, v8, s[12:13]
	v_cmp_le_u32_e64 s[12:13], s6, v193
	v_addc_co_u32_e64 v8, s[20:21], 0, v8, s[16:17]
	v_cmp_le_u32_e64 s[16:17], s6, v194
	v_addc_co_u32_e64 v8, s[20:21], 0, v8, s[8:9]
	v_addc_co_u32_e64 v8, s[20:21], 0, v8, s[12:13]
	v_addc_co_u32_e64 v8, s[20:21], 0, v8, s[16:17]
	v_and_b32_e32 v9, 8, v8
	v_cmp_ne_u32_e64 s[18:19], 0, v9
	v_and_b32_e32 v9, 4, v8
	v_cmp_ne_u32_e64 s[16:17], 0, v9
	v_and_b32_e32 v9, 2, v8
	v_cmp_ne_u32_e64 s[12:13], 0, v9
	v_and_b32_e32 v9, 1, v8
	v_cmp_ne_u32_e64 s[8:9], 0, v9
	s_bcnt1_i32_b64 s7, s[18:19]
	s_bcnt1_i32_b64 s3, s[16:17]
	s_lshl1_add_u32 s7, s7, s3
	s_bcnt1_i32_b64 s3, s[12:13]
	s_lshl1_add_u32 s7, s7, s3
	s_bcnt1_i32_b64 s3, s[8:9]
	s_lshl1_add_u32 s7, s7, s3
	s_cmpk_lt_u32 s7, 0x100
	s_cselect_b32 s4, s4, s6
	s_cmpk_eq_u32 s7, 0x100
	s_cbranch_scc1 .Ltk0_x12
	s_lshr_b32 s5, s5, 1
	s_cbranch_scc1 .Ltk0_l12
	s_branch .Ltk0_orig

.Ltk0_x28:
	v_cmp_le_u32_e64 s[8:9], s4, v172
	v_cmp_le_u32_e64 s[12:13], s4, v179
	v_cmp_le_u32_e64 s[16:17], s4, v181
	s_nop 0
	v_writelane_b32 v10, s8, 0
	v_writelane_b32 v11, s9, 0
	v_cmp_le_u32_e64 s[8:9], s4, v183
	v_writelane_b32 v10, s12, 1
	v_writelane_b32 v11, s13, 1
	v_cmp_le_u32_e64 s[12:13], s4, v185
	v_writelane_b32 v10, s16, 2
	v_writelane_b32 v11, s17, 2
	v_cmp_le_u32_e64 s[16:17], s4, v187
	v_writelane_b32 v10, s8, 3
	v_writelane_b32 v11, s9, 3
	v_cmp_le_u32_e64 s[8:9], s4, v189
	v_writelane_b32 v10, s12, 4
	v_writelane_b32 v11, s13, 4
	v_cmp_le_u32_e64 s[12:13], s4, v190
	v_writelane_b32 v10, s16, 5
	v_writelane_b32 v11, s17, 5
	v_cmp_le_u32_e64 s[16:17], s4, v191
	v_writelane_b32 v10, s8, 6
	v_writelane_b32 v11, s9, 6
	v_cmp_le_u32_e64 s[8:9], s4, v192
	v_writelane_b32 v10, s12, 7
	v_writelane_b32 v11, s13, 7
	v_cmp_le_u32_e64 s[12:13], s4, v193
	v_writelane_b32 v10, s16, 8
	v_writelane_b32 v11, s17, 8
	v_cmp_le_u32_e64 s[16:17], s4, v194
	v_writelane_b32 v10, s8, 9
	v_writelane_b32 v11, s9, 9
	v_cmp_le_u32_e64 s[8:9], s4, v195
	v_writelane_b32 v10, s12, 10
	v_writelane_b32 v11, s13, 10
	v_cmp_le_u32_e64 s[12:13], s4, v196
	v_writelane_b32 v10, s16, 11
	v_writelane_b32 v11, s17, 11
	v_cmp_le_u32_e64 s[16:17], s4, v198
	v_writelane_b32 v10, s8, 12
	v_writelane_b32 v11, s9, 12
	v_cmp_le_u32_e64 s[8:9], s4, v200
	v_writelane_b32 v10, s12, 13
	v_writelane_b32 v11, s13, 13
	v_cmp_le_u32_e64 s[12:13], s4, v206
	v_writelane_b32 v10, s16, 14
	v_writelane_b32 v11, s17, 14
	v_cmp_le_u32_e64 s[16:17], s4, v207
	v_writelane_b32 v10, s8, 15
	v_writelane_b32 v11, s9, 15
	v_cmp_le_u32_e64 s[8:9], s4, v208
	v_writelane_b32 v10, s12, 16
	v_writelane_b32 v11, s13, 16
	v_cmp_le_u32_e64 s[12:13], s4, v209
	v_writelane_b32 v10, s16, 17
	v_writelane_b32 v11, s17, 17
	v_cmp_le_u32_e64 s[16:17], s4, v210
	v_writelane_b32 v10, s8, 18
	v_writelane_b32 v11, s9, 18
	v_cmp_le_u32_e64 s[8:9], s4, v211
	v_writelane_b32 v10, s12, 19
	v_writelane_b32 v11, s13, 19
	v_cmp_le_u32_e64 s[12:13], s4, v212
	v_writelane_b32 v10, s16, 20
	v_writelane_b32 v11, s17, 20
	v_cmp_le_u32_e64 s[16:17], s4, v213
	v_writelane_b32 v10, s8, 21
	v_writelane_b32 v11, s9, 21
	v_cmp_le_u32_e64 s[8:9], s4, v214
	v_writelane_b32 v10, s12, 22
	v_writelane_b32 v11, s13, 22
	v_cmp_le_u32_e64 s[12:13], s4, v215
	v_writelane_b32 v10, s16, 23
	v_writelane_b32 v11, s17, 23
	v_cmp_le_u32_e64 s[16:17], s4, v216
	v_writelane_b32 v10, s8, 24
	v_writelane_b32 v11, s9, 24
	v_cmp_le_u32_e64 s[8:9], s4, v217
	v_writelane_b32 v10, s12, 25
	v_writelane_b32 v11, s13, 25
	v_writelane_b32 v10, s16, 26
	v_writelane_b32 v11, s17, 26
	v_writelane_b32 v10, s8, 27
	v_writelane_b32 v11, s9, 27
	v_mov_b32_e32 v2, v10
	v_mov_b32_e32 v3, v11
	s_branch .LBB0_1883

.Ltk0_x20:
	v_cmp_le_u32_e64 s[8:9], s4, v172
	v_cmp_le_u32_e64 s[12:13], s4, v179
	v_cmp_le_u32_e64 s[16:17], s4, v181
	s_nop 0
	v_writelane_b32 v10, s8, 0
	v_writelane_b32 v11, s9, 0
	v_cmp_le_u32_e64 s[8:9], s4, v183
	v_writelane_b32 v10, s12, 1
	v_writelane_b32 v11, s13, 1
	v_cmp_le_u32_e64 s[12:13], s4, v185
	v_writelane_b32 v10, s16, 2
	v_writelane_b32 v11, s17, 2
	v_cmp_le_u32_e64 s[16:17], s4, v187
	v_writelane_b32 v10, s8, 3
	v_writelane_b32 v11, s9, 3
	v_cmp_le_u32_e64 s[8:9], s4, v189
	v_writelane_b32 v10, s12, 4
	v_writelane_b32 v11, s13, 4
	v_cmp_le_u32_e64 s[12:13], s4, v190
	v_writelane_b32 v10, s16, 5
	v_writelane_b32 v11, s17, 5
	v_cmp_le_u32_e64 s[16:17], s4, v191
	v_writelane_b32 v10, s8, 6
	v_writelane_b32 v11, s9, 6
	v_cmp_le_u32_e64 s[8:9], s4, v192
	v_writelane_b32 v10, s12, 7
	v_writelane_b32 v11, s13, 7
	v_cmp_le_u32_e64 s[12:13], s4, v193
	v_writelane_b32 v10, s16, 8
	v_writelane_b32 v11, s17, 8
	v_cmp_le_u32_e64 s[16:17], s4, v194
	v_writelane_b32 v10, s8, 9
	v_writelane_b32 v11, s9, 9
	v_cmp_le_u32_e64 s[8:9], s4, v195
	v_writelane_b32 v10, s12, 10
	v_writelane_b32 v11, s13, 10
	v_cmp_le_u32_e64 s[12:13], s4, v196
	v_writelane_b32 v10, s16, 11
	v_writelane_b32 v11, s17, 11
	v_cmp_le_u32_e64 s[16:17], s4, v198
	v_writelane_b32 v10, s8, 12
	v_writelane_b32 v11, s9, 12
	v_cmp_le_u32_e64 s[8:9], s4, v200
	v_writelane_b32 v10, s12, 13
	v_writelane_b32 v11, s13, 13
	v_cmp_le_u32_e64 s[12:13], s4, v206
	v_writelane_b32 v10, s16, 14
	v_writelane_b32 v11, s17, 14
	v_cmp_le_u32_e64 s[16:17], s4, v207
	v_writelane_b32 v10, s8, 15
	v_writelane_b32 v11, s9, 15
	v_cmp_le_u32_e64 s[8:9], s4, v208
	v_writelane_b32 v10, s12, 16
	v_writelane_b32 v11, s13, 16
	v_cmp_le_u32_e64 s[12:13], s4, v209
	v_writelane_b32 v10, s16, 17
	v_writelane_b32 v11, s17, 17
	v_writelane_b32 v10, s8, 18
	v_writelane_b32 v11, s9, 18
	v_writelane_b32 v10, s12, 19
	v_writelane_b32 v11, s13, 19
	v_mov_b32_e32 v2, v10
	v_mov_b32_e32 v3, v11
	s_branch .LBB0_1883

.Ltk0_x12:
	v_cmp_le_u32_e64 s[8:9], s4, v172
	v_cmp_le_u32_e64 s[12:13], s4, v179
	v_cmp_le_u32_e64 s[16:17], s4, v181
	s_nop 0
	v_writelane_b32 v10, s8, 0
	v_writelane_b32 v11, s9, 0
	v_cmp_le_u32_e64 s[8:9], s4, v183
	v_writelane_b32 v10, s12, 1
	v_writelane_b32 v11, s13, 1
	v_cmp_le_u32_e64 s[12:13], s4, v185
	v_writelane_b32 v10, s16, 2
	v_writelane_b32 v11, s17, 2
	v_cmp_le_u32_e64 s[16:17], s4, v187
	v_writelane_b32 v10, s8, 3
	v_writelane_b32 v11, s9, 3
	v_cmp_le_u32_e64 s[8:9], s4, v189
	v_writelane_b32 v10, s12, 4
	v_writelane_b32 v11, s13, 4
	v_cmp_le_u32_e64 s[12:13], s4, v190
	v_writelane_b32 v10, s16, 5
	v_writelane_b32 v11, s17, 5
	v_cmp_le_u32_e64 s[16:17], s4, v191
	v_writelane_b32 v10, s8, 6
	v_writelane_b32 v11, s9, 6
	v_cmp_le_u32_e64 s[8:9], s4, v192
	v_writelane_b32 v10, s12, 7
	v_writelane_b32 v11, s13, 7
	v_cmp_le_u32_e64 s[12:13], s4, v193
	v_writelane_b32 v10, s16, 8
	v_writelane_b32 v11, s17, 8
	v_cmp_le_u32_e64 s[16:17], s4, v194
	v_writelane_b32 v10, s8, 9
	v_writelane_b32 v11, s9, 9
	v_writelane_b32 v10, s12, 10
	v_writelane_b32 v11, s13, 10
	v_writelane_b32 v10, s16, 11
	v_writelane_b32 v11, s17, 11
	v_mov_b32_e32 v2, v10
	v_mov_b32_e32 v3, v11
	s_branch .LBB0_1883

.LBB0_1886:
	s_or_b64 exec, exec, s[0:1]
	s_cmp_lt_u32 s33, 4
	s_cbranch_scc1 .Ltk1_orig
	s_mov_b32 s4, 0
	s_mov_b32 s5, 0x80000000
	s_cmp_lt_u32 s33, 8
	s_cbranch_scc1 .Ltk1_l8
	s_cmp_lt_u32 s33, 12
	s_cbranch_scc1 .Ltk1_l12
	s_cmp_lt_u32 s33, 16
	s_cbranch_scc1 .Ltk1_l16
	s_cmp_lt_u32 s33, 20
	s_cbranch_scc1 .Ltk1_l20
	s_cmp_lt_u32 s33, 24
	s_cbranch_scc1 .Ltk1_l24
	s_cmp_lt_u32 s33, 28
	s_cbranch_scc1 .Ltk1_l28

.Ltk1_l28:
	s_or_b32 s6, s4, s5
	v_cmp_le_u32_e64 s[8:9], s6, v140
	v_cmp_le_u32_e64 s[12:13], s6, v142
	v_cmp_le_u32_e64 s[16:17], s6, v144
	v_cndmask_b32_e64 v8, 0, 1, s[8:9]
	v_cmp_le_u32_e64 s[8:9], s6, v146
	v_addc_co_u32_e64 v8, s[20:21], 0, v8, s[12:13]
	v_cmp_le_u32_e64 s[12:13], s6, v148
	v_addc_co_u32_e64 v8, s[20:21], 0, v8, s[16:17]
	v_cmp_le_u32_e64 s[16:17], s6, v150
	v_addc_co_u32_e64 v8, s[20:21], 0, v8, s[8:9]
	v_cmp_le_u32_e64 s[8:9], s6, v152
	v_addc_co_u32_e64 v8, s[20:21], 0, v8, s[12:13]
	v_cmp_le_u32_e64 s[12:13], s6, v153
	v_addc_co_u32_e64 v8, s[20:21], 0, v8, s[16:17]
	v_cmp_le_u32_e64 s[16:17], s6, v154
	v_addc_co_u32_e64 v8, s[20:21], 0, v8, s[8:9]
	v_cmp_le_u32_e64 s[8:9], s6, v155
	v_addc_co_u32_e64 v8, s[20:21], 0, v8, s[12:13]
	v_cmp_le_u32_e64 s[12:13], s6, v156
	v_addc_co_u32_e64 v8, s[20:21], 0, v8, s[16:17]
	v_cmp_le_u32_e64 s[16:17], s6, v157
	v_addc_co_u32_e64 v8, s[20:21], 0, v8, s[8:9]
	v_cmp_le_u32_e64 s[8:9], s6, v158
	v_addc_co_u32_e64 v8, s[20:21], 0, v8, s[12:13]
	v_cmp_le_u32_e64 s[12:13], s6, v159
	v_addc_co_u32_e64 v8, s[20:21], 0, v8, s[16:17]
	v_cmp_le_u32_e64 s[16:17], s6, v161
	v_addc_co_u32_e64 v8, s[20:21], 0, v8, s[8:9]
	v_cmp_le_u32_e64 s[8:9], s6, v164
	v_addc_co_u32_e64 v8, s[20:21], 0, v8, s[12:13]
	v_cmp_le_u32_e64 s[12:13], s6, v170
	v_addc_co_u32_e64 v8, s[20:21], 0, v8, s[16:17]
	v_cmp_le_u32_e64 s[16:17], s6, v171
	v_addc_co_u32_e64 v8, s[20:21], 0, v8, s[8:9]
	v_cmp_le_u32_e64 s[8:9], s6, v173
	v_addc_co_u32_e64 v8, s[20:21], 0, v8, s[12:13]
	v_cmp_le_u32_e64 s[12:13], s6, v180
	v_addc_co_u32_e64 v8, s[20:21], 0, v8, s[16:17]
	v_cmp_le_u32_e64 s[16:17], s6, v182
	v_addc_co_u32_e64 v8, s[20:21], 0, v8, s[8:9]
	v_cmp_le_u32_e64 s[8:9], s6, v184
	v_addc_co_u32_e64 v8, s[20:21], 0, v8, s[12:13]
	v_cmp_le_u32_e64 s[12:13], s6, v186
	v_addc_co_u32_e64 v8, s[20:21], 0, v8, s[16:17]
	v_cmp_le_u32_e64 s[16:17], s6, v188
	v_addc_co_u32_e64 v8, s[20:21], 0, v8, s[8:9]
	v_cmp_le_u32_e64 s[8:9], s6, v197
	v_addc_co_u32_e64 v8, s[20:21], 0, v8, s[12:13]
	v_cmp_le_u32_e64 s[12:13], s6, v199
	v_addc_co_u32_e64 v8, s[20:21], 0, v8, s[16:17]
	v_cmp_le_u32_e64 s[16:17], s6, v201
	v_addc_co_u32_e64 v8, s[20:21], 0, v8, s[8:9]
	v_cmp_le_u32_e64 s[8:9], s6, v202
	v_addc_co_u32_e64 v8, s[20:21], 0, v8, s[12:13]
	v_addc_co_u32_e64 v8, s[20:21], 0, v8, s[16:17]
	v_addc_co_u32_e64 v8, s[20:21], 0, v8, s[8:9]
	v_and_b32_e32 v9, 16, v8
	v_cmp_ne_u32_e64 s[22:23], 0, v9
	v_and_b32_e32 v9, 8, v8
	v_cmp_ne_u32_e64 s[18:19], 0, v9
	v_and_b32_e32 v9, 4, v8
	v_cmp_ne_u32_e64 s[16:17], 0, v9
	v_and_b32_e32 v9, 2, v8
	v_cmp_ne_u32_e64 s[12:13], 0, v9
	v_and_b32_e32 v9, 1, v8
	v_cmp_ne_u32_e64 s[8:9], 0, v9
	s_bcnt1_i32_b64 s7, s[22:23]
	s_bcnt1_i32_b64 s3, s[18:19]
	s_lshl1_add_u32 s7, s7, s3
	s_bcnt1_i32_b64 s3, s[16:17]
	s_lshl1_add_u32 s7, s7, s3
	s_bcnt1_i32_b64 s3, s[12:13]
	s_lshl1_add_u32 s7, s7, s3
	s_bcnt1_i32_b64 s3, s[8:9]
	s_lshl1_add_u32 s7, s7, s3
	s_cmpk_lt_u32 s7, 0x100
	s_cselect_b32 s4, s4, s6
	s_cmpk_eq_u32 s7, 0x100
	s_cbranch_scc1 .Ltk1_x28
	s_lshr_b32 s5, s5, 1
	s_cbranch_scc1 .Ltk1_l28
	s_branch .Ltk1_orig

.Ltk1_l20:
	s_or_b32 s6, s4, s5
	v_cmp_le_u32_e64 s[8:9], s6, v140
	v_cmp_le_u32_e64 s[12:13], s6, v142
	v_cmp_le_u32_e64 s[16:17], s6, v144
	v_cndmask_b32_e64 v8, 0, 1, s[8:9]
	v_cmp_le_u32_e64 s[8:9], s6, v146
	v_addc_co_u32_e64 v8, s[20:21], 0, v8, s[12:13]
	v_cmp_le_u32_e64 s[12:13], s6, v148
	v_addc_co_u32_e64 v8, s[20:21], 0, v8, s[16:17]
	v_cmp_le_u32_e64 s[16:17], s6, v150
	v_addc_co_u32_e64 v8, s[20:21], 0, v8, s[8:9]
	v_cmp_le_u32_e64 s[8:9], s6, v152
	v_addc_co_u32_e64 v8, s[20:21], 0, v8, s[12:13]
	v_cmp_le_u32_e64 s[12:13], s6, v153
	v_addc_co_u32_e64 v8, s[20:21], 0, v8, s[16:17]
	v_cmp_le_u32_e64 s[16:17], s6, v154
	v_addc_co_u32_e64 v8, s[20:21], 0, v8, s[8:9]
	v_cmp_le_u32_e64 s[8:9], s6, v155
	v_addc_co_u32_e64 v8, s[20:21], 0, v8, s[12:13]
	v_cmp_le_u32_e64 s[12:13], s6, v156
	v_addc_co_u32_e64 v8, s[20:21], 0, v8, s[16:17]
	v_cmp_le_u32_e64 s[16:17], s6, v157
	v_addc_co_u32_e64 v8, s[20:21], 0, v8, s[8:9]
	v_cmp_le_u32_e64 s[8:9], s6, v158
	v_addc_co_u32_e64 v8, s[20:21], 0, v8, s[12:13]
	v_cmp_le_u32_e64 s[12:13], s6, v159
	v_addc_co_u32_e64 v8, s[20:21], 0, v8, s[16:17]
	v_cmp_le_u32_e64 s[16:17], s6, v161
	v_addc_co_u32_e64 v8, s[20:21], 0, v8, s[8:9]
	v_cmp_le_u32_e64 s[8:9], s6, v164
	v_addc_co_u32_e64 v8, s[20:21], 0, v8, s[12:13]
	v_cmp_le_u32_e64 s[12:13], s6, v170
	v_addc_co_u32_e64 v8, s[20:21], 0, v8, s[16:17]
	v_cmp_le_u32_e64 s[16:17], s6, v171
	v_addc_co_u32_e64 v8, s[20:21], 0, v8, s[8:9]
	v_cmp_le_u32_e64 s[8:9], s6, v173
	v_addc_co_u32_e64 v8, s[20:21], 0, v8, s[12:13]
	v_cmp_le_u32_e64 s[12:13], s6, v180
	v_addc_co_u32_e64 v8, s[20:21], 0, v8, s[16:17]
	v_addc_co_u32_e64 v8, s[20:21], 0, v8, s[8:9]
	v_addc_co_u32_e64 v8, s[20:21], 0, v8, s[12:13]
	v_and_b32_e32 v9, 16, v8
	v_cmp_ne_u32_e64 s[22:23], 0, v9
	v_and_b32_e32 v9, 8, v8
	v_cmp_ne_u32_e64 s[18:19], 0, v9
	v_and_b32_e32 v9, 4, v8
	v_cmp_ne_u32_e64 s[16:17], 0, v9
	v_and_b32_e32 v9, 2, v8
	v_cmp_ne_u32_e64 s[12:13], 0, v9
	v_and_b32_e32 v9, 1, v8
	v_cmp_ne_u32_e64 s[8:9], 0, v9
	s_bcnt1_i32_b64 s7, s[22:23]
	s_bcnt1_i32_b64 s3, s[18:19]
	s_lshl1_add_u32 s7, s7, s3
	s_bcnt1_i32_b64 s3, s[16:17]
	s_lshl1_add_u32 s7, s7, s3
	s_bcnt1_i32_b64 s3, s[12:13]
	s_lshl1_add_u32 s7, s7, s3
	s_bcnt1_i32_b64 s3, s[8:9]
	s_lshl1_add_u32 s7, s7, s3
	s_cmpk_lt_u32 s7, 0x100
	s_cselect_b32 s4, s4, s6
	s_cmpk_eq_u32 s7, 0x100
	s_cbranch_scc1 .Ltk1_x20
	s_lshr_b32 s5, s5, 1
	s_cbranch_scc1 .Ltk1_l20
	s_branch .Ltk1_orig

.Ltk1_l12:
	s_or_b32 s6, s4, s5
	v_cmp_le_u32_e64 s[8:9], s6, v140
	v_cmp_le_u32_e64 s[12:13], s6, v142
	v_cmp_le_u32_e64 s[16:17], s6, v144
	v_cndmask_b32_e64 v8, 0, 1, s[8:9]
	v_cmp_le_u32_e64 s[8:9], s6, v146
	v_addc_co_u32_e64 v8, s[20:21], 0, v8, s[12:13]
	v_cmp_le_u32_e64 s[12:13], s6, v148
	v_addc_co_u32_e64 v8, s[20:21], 0, v8, s[16:17]
	v_cmp_le_u32_e64 s[16:17], s6, v150
	v_addc_co_u32_e64 v8, s[20:21], 0, v8, s[8:9]
	v_cmp_le_u32_e64 s[8:9], s6, v152
	v_addc_co_u32_e64 v8, s[20:21], 0, v8, s[12:13]
	v_cmp_le_u32_e64 s[12:13], s6, v153
	v_addc_co_u32_e64 v8, s[20:21], 0, v8, s[16:17]
	v_cmp_le_u32_e64 s[16:17], s6, v154
	v_addc_co_u32_e64 v8, s[20:21], 0, v8, s[8:9]
	v_cmp_le_u32_e64 s[8:9], s6, v155
	v_addc_co_u32_e64 v8, s[20:21], 0, v8, s[12:13]
	v_cmp_le_u32_e64 s[12:13], s6, v156
	v_addc_co_u32_e64 v8, s[20:21], 0, v8, s[16:17]
	v_cmp_le_u32_e64 s[16:17], s6, v157
	v_addc_co_u32_e64 v8, s[20:21], 0, v8, s[8:9]
	v_addc_co_u32_e64 v8, s[20:21], 0, v8, s[12:13]
	v_addc_co_u32_e64 v8, s[20:21], 0, v8, s[16:17]
	v_and_b32_e32 v9, 8, v8
	v_cmp_ne_u32_e64 s[18:19], 0, v9
	v_and_b32_e32 v9, 4, v8
	v_cmp_ne_u32_e64 s[16:17], 0, v9
	v_and_b32_e32 v9, 2, v8
	v_cmp_ne_u32_e64 s[12:13], 0, v9
	v_and_b32_e32 v9, 1, v8
	v_cmp_ne_u32_e64 s[8:9], 0, v9
	s_bcnt1_i32_b64 s7, s[18:19]
	s_bcnt1_i32_b64 s3, s[16:17]
	s_lshl1_add_u32 s7, s7, s3
	s_bcnt1_i32_b64 s3, s[12:13]
	s_lshl1_add_u32 s7, s7, s3
	s_bcnt1_i32_b64 s3, s[8:9]
	s_lshl1_add_u32 s7, s7, s3
	s_cmpk_lt_u32 s7, 0x100
	s_cselect_b32 s4, s4, s6
	s_cmpk_eq_u32 s7, 0x100
	s_cbranch_scc1 .Ltk1_x12
	s_lshr_b32 s5, s5, 1
	s_cbranch_scc1 .Ltk1_l12
	s_branch .Ltk1_orig

.Ltk1_x28:
	v_cmp_le_u32_e64 s[8:9], s4, v140
	v_cmp_le_u32_e64 s[12:13], s4, v142
	v_cmp_le_u32_e64 s[16:17], s4, v144
	s_nop 0
	v_writelane_b32 v10, s8, 0
	v_writelane_b32 v11, s9, 0
	v_cmp_le_u32_e64 s[8:9], s4, v146
	v_writelane_b32 v10, s12, 1
	v_writelane_b32 v11, s13, 1
	v_cmp_le_u32_e64 s[12:13], s4, v148
	v_writelane_b32 v10, s16, 2
	v_writelane_b32 v11, s17, 2
	v_cmp_le_u32_e64 s[16:17], s4, v150
	v_writelane_b32 v10, s8, 3
	v_writelane_b32 v11, s9, 3
	v_cmp_le_u32_e64 s[8:9], s4, v152
	v_writelane_b32 v10, s12, 4
	v_writelane_b32 v11, s13, 4
	v_cmp_le_u32_e64 s[12:13], s4, v153
	v_writelane_b32 v10, s16, 5
	v_writelane_b32 v11, s17, 5
	v_cmp_le_u32_e64 s[16:17], s4, v154
	v_writelane_b32 v10, s8, 6
	v_writelane_b32 v11, s9, 6
	v_cmp_le_u32_e64 s[8:9], s4, v155
	v_writelane_b32 v10, s12, 7
	v_writelane_b32 v11, s13, 7
	v_cmp_le_u32_e64 s[12:13], s4, v156
	v_writelane_b32 v10, s16, 8
	v_writelane_b32 v11, s17, 8
	v_cmp_le_u32_e64 s[16:17], s4, v157
	v_writelane_b32 v10, s8, 9
	v_writelane_b32 v11, s9, 9
	v_cmp_le_u32_e64 s[8:9], s4, v158
	v_writelane_b32 v10, s12, 10
	v_writelane_b32 v11, s13, 10
	v_cmp_le_u32_e64 s[12:13], s4, v159
	v_writelane_b32 v10, s16, 11
	v_writelane_b32 v11, s17, 11
	v_cmp_le_u32_e64 s[16:17], s4, v161
	v_writelane_b32 v10, s8, 12
	v_writelane_b32 v11, s9, 12
	v_cmp_le_u32_e64 s[8:9], s4, v164
	v_writelane_b32 v10, s12, 13
	v_writelane_b32 v11, s13, 13
	v_cmp_le_u32_e64 s[12:13], s4, v170
	v_writelane_b32 v10, s16, 14
	v_writelane_b32 v11, s17, 14
	v_cmp_le_u32_e64 s[16:17], s4, v171
	v_writelane_b32 v10, s8, 15
	v_writelane_b32 v11, s9, 15
	v_cmp_le_u32_e64 s[8:9], s4, v173
	v_writelane_b32 v10, s12, 16
	v_writelane_b32 v11, s13, 16
	v_cmp_le_u32_e64 s[12:13], s4, v180
	v_writelane_b32 v10, s16, 17
	v_writelane_b32 v11, s17, 17
	v_cmp_le_u32_e64 s[16:17], s4, v182
	v_writelane_b32 v10, s8, 18
	v_writelane_b32 v11, s9, 18
	v_cmp_le_u32_e64 s[8:9], s4, v184
	v_writelane_b32 v10, s12, 19
	v_writelane_b32 v11, s13, 19
	v_cmp_le_u32_e64 s[12:13], s4, v186
	v_writelane_b32 v10, s16, 20
	v_writelane_b32 v11, s17, 20
	v_cmp_le_u32_e64 s[16:17], s4, v188
	v_writelane_b32 v10, s8, 21
	v_writelane_b32 v11, s9, 21
	v_cmp_le_u32_e64 s[8:9], s4, v197
	v_writelane_b32 v10, s12, 22
	v_writelane_b32 v11, s13, 22
	v_cmp_le_u32_e64 s[12:13], s4, v199
	v_writelane_b32 v10, s16, 23
	v_writelane_b32 v11, s17, 23
	v_cmp_le_u32_e64 s[16:17], s4, v201
	v_writelane_b32 v10, s8, 24
	v_writelane_b32 v11, s9, 24
	v_cmp_le_u32_e64 s[8:9], s4, v202
	v_writelane_b32 v10, s12, 25
	v_writelane_b32 v11, s13, 25
	v_writelane_b32 v10, s16, 26
	v_writelane_b32 v11, s17, 26
	v_writelane_b32 v10, s8, 27
	v_writelane_b32 v11, s9, 27
	v_mov_b32_e32 v2, v10
	v_mov_b32_e32 v3, v11
	s_branch .LBB0_2149

.Ltk1_x20:
	v_cmp_le_u32_e64 s[8:9], s4, v140
	v_cmp_le_u32_e64 s[12:13], s4, v142
	v_cmp_le_u32_e64 s[16:17], s4, v144
	s_nop 0
	v_writelane_b32 v10, s8, 0
	v_writelane_b32 v11, s9, 0
	v_cmp_le_u32_e64 s[8:9], s4, v146
	v_writelane_b32 v10, s12, 1
	v_writelane_b32 v11, s13, 1
	v_cmp_le_u32_e64 s[12:13], s4, v148
	v_writelane_b32 v10, s16, 2
	v_writelane_b32 v11, s17, 2
	v_cmp_le_u32_e64 s[16:17], s4, v150
	v_writelane_b32 v10, s8, 3
	v_writelane_b32 v11, s9, 3
	v_cmp_le_u32_e64 s[8:9], s4, v152
	v_writelane_b32 v10, s12, 4
	v_writelane_b32 v11, s13, 4
	v_cmp_le_u32_e64 s[12:13], s4, v153
	v_writelane_b32 v10, s16, 5
	v_writelane_b32 v11, s17, 5
	v_cmp_le_u32_e64 s[16:17], s4, v154
	v_writelane_b32 v10, s8, 6
	v_writelane_b32 v11, s9, 6
	v_cmp_le_u32_e64 s[8:9], s4, v155
	v_writelane_b32 v10, s12, 7
	v_writelane_b32 v11, s13, 7
	v_cmp_le_u32_e64 s[12:13], s4, v156
	v_writelane_b32 v10, s16, 8
	v_writelane_b32 v11, s17, 8
	v_cmp_le_u32_e64 s[16:17], s4, v157
	v_writelane_b32 v10, s8, 9
	v_writelane_b32 v11, s9, 9
	v_cmp_le_u32_e64 s[8:9], s4, v158
	v_writelane_b32 v10, s12, 10
	v_writelane_b32 v11, s13, 10
	v_cmp_le_u32_e64 s[12:13], s4, v159
	v_writelane_b32 v10, s16, 11
	v_writelane_b32 v11, s17, 11
	v_cmp_le_u32_e64 s[16:17], s4, v161
	v_writelane_b32 v10, s8, 12
	v_writelane_b32 v11, s9, 12
	v_cmp_le_u32_e64 s[8:9], s4, v164
	v_writelane_b32 v10, s12, 13
	v_writelane_b32 v11, s13, 13
	v_cmp_le_u32_e64 s[12:13], s4, v170
	v_writelane_b32 v10, s16, 14
	v_writelane_b32 v11, s17, 14
	v_cmp_le_u32_e64 s[16:17], s4, v171
	v_writelane_b32 v10, s8, 15
	v_writelane_b32 v11, s9, 15
	v_cmp_le_u32_e64 s[8:9], s4, v173
	v_writelane_b32 v10, s12, 16
	v_writelane_b32 v11, s13, 16
	v_cmp_le_u32_e64 s[12:13], s4, v180
	v_writelane_b32 v10, s16, 17
	v_writelane_b32 v11, s17, 17
	v_writelane_b32 v10, s8, 18
	v_writelane_b32 v11, s9, 18
	v_writelane_b32 v10, s12, 19
	v_writelane_b32 v11, s13, 19
	v_mov_b32_e32 v2, v10
	v_mov_b32_e32 v3, v11
	s_branch .LBB0_2149

.Ltk1_x12:
	v_cmp_le_u32_e64 s[8:9], s4, v140
	v_cmp_le_u32_e64 s[12:13], s4, v142
	v_cmp_le_u32_e64 s[16:17], s4, v144
	s_nop 0
	v_writelane_b32 v10, s8, 0
	v_writelane_b32 v11, s9, 0
	v_cmp_le_u32_e64 s[8:9], s4, v146
	v_writelane_b32 v10, s12, 1
	v_writelane_b32 v11, s13, 1
	v_cmp_le_u32_e64 s[12:13], s4, v148
	v_writelane_b32 v10, s16, 2
	v_writelane_b32 v11, s17, 2
	v_cmp_le_u32_e64 s[16:17], s4, v150
	v_writelane_b32 v10, s8, 3
	v_writelane_b32 v11, s9, 3
	v_cmp_le_u32_e64 s[8:9], s4, v152
	v_writelane_b32 v10, s12, 4
	v_writelane_b32 v11, s13, 4
	v_cmp_le_u32_e64 s[12:13], s4, v153
	v_writelane_b32 v10, s16, 5
	v_writelane_b32 v11, s17, 5
	v_cmp_le_u32_e64 s[16:17], s4, v154
	v_writelane_b32 v10, s8, 6
	v_writelane_b32 v11, s9, 6
	v_cmp_le_u32_e64 s[8:9], s4, v155
	v_writelane_b32 v10, s12, 7
	v_writelane_b32 v11, s13, 7
	v_cmp_le_u32_e64 s[12:13], s4, v156
	v_writelane_b32 v10, s16, 8
	v_writelane_b32 v11, s17, 8
	v_cmp_le_u32_e64 s[16:17], s4, v157
	v_writelane_b32 v10, s8, 9
	v_writelane_b32 v11, s9, 9
	v_writelane_b32 v10, s12, 10
	v_writelane_b32 v11, s13, 10
	v_writelane_b32 v10, s16, 11
	v_writelane_b32 v11, s17, 11
	v_mov_b32_e32 v2, v10
	v_mov_b32_e32 v3, v11
	s_branch .LBB0_2149

.Ltk2_l28:
	s_or_b32 s6, s4, s5
	v_cmp_le_u32_e64 s[8:9], s6, v111
	v_cmp_le_u32_e64 s[12:13], s6, v113
	v_cmp_le_u32_e64 s[16:17], s6, v115
	v_cndmask_b32_e64 v8, 0, 1, s[8:9]
	v_cmp_le_u32_e64 s[8:9], s6, v117
	v_addc_co_u32_e64 v8, s[20:21], 0, v8, s[12:13]
	v_cmp_le_u32_e64 s[12:13], s6, v119
	v_addc_co_u32_e64 v8, s[20:21], 0, v8, s[16:17]
	v_cmp_le_u32_e64 s[16:17], s6, v121
	v_addc_co_u32_e64 v8, s[20:21], 0, v8, s[8:9]
	v_cmp_le_u32_e64 s[8:9], s6, v123
	v_addc_co_u32_e64 v8, s[20:21], 0, v8, s[12:13]
	v_cmp_le_u32_e64 s[12:13], s6, v124
	v_addc_co_u32_e64 v8, s[20:21], 0, v8, s[16:17]
	v_cmp_le_u32_e64 s[16:17], s6, v125
	v_addc_co_u32_e64 v8, s[20:21], 0, v8, s[8:9]
	v_cmp_le_u32_e64 s[8:9], s6, v126
	v_addc_co_u32_e64 v8, s[20:21], 0, v8, s[12:13]
	v_cmp_le_u32_e64 s[12:13], s6, v127
	v_addc_co_u32_e64 v8, s[20:21], 0, v8, s[16:17]
	v_cmp_le_u32_e64 s[16:17], s6, v128
	v_addc_co_u32_e64 v8, s[20:21], 0, v8, s[8:9]
	v_cmp_le_u32_e64 s[8:9], s6, v129
	v_addc_co_u32_e64 v8, s[20:21], 0, v8, s[12:13]
	v_cmp_le_u32_e64 s[12:13], s6, v130
	v_addc_co_u32_e64 v8, s[20:21], 0, v8, s[16:17]
	v_cmp_le_u32_e64 s[16:17], s6, v132
	v_addc_co_u32_e64 v8, s[20:21], 0, v8, s[8:9]
	v_cmp_le_u32_e64 s[8:9], s6, v133
	v_addc_co_u32_e64 v8, s[20:21], 0, v8, s[12:13]
	v_cmp_le_u32_e64 s[12:13], s6, v138
	v_addc_co_u32_e64 v8, s[20:21], 0, v8, s[16:17]
	v_cmp_le_u32_e64 s[16:17], s6, v139
	v_addc_co_u32_e64 v8, s[20:21], 0, v8, s[8:9]
	v_cmp_le_u32_e64 s[8:9], s6, v141
	v_addc_co_u32_e64 v8, s[20:21], 0, v8, s[12:13]
	v_cmp_le_u32_e64 s[12:13], s6, v143
	v_addc_co_u32_e64 v8, s[20:21], 0, v8, s[16:17]
	v_cmp_le_u32_e64 s[16:17], s6, v145
	v_addc_co_u32_e64 v8, s[20:21], 0, v8, s[8:9]
	v_cmp_le_u32_e64 s[8:9], s6, v147
	v_addc_co_u32_e64 v8, s[20:21], 0, v8, s[12:13]
	v_cmp_le_u32_e64 s[12:13], s6, v149
	v_addc_co_u32_e64 v8, s[20:21], 0, v8, s[16:17]
	v_cmp_le_u32_e64 s[16:17], s6, v151
	v_addc_co_u32_e64 v8, s[20:21], 0, v8, s[8:9]
	v_cmp_le_u32_e64 s[8:9], s6, v160
	v_addc_co_u32_e64 v8, s[20:21], 0, v8, s[12:13]
	v_cmp_le_u32_e64 s[12:13], s6, v163
	v_addc_co_u32_e64 v8, s[20:21], 0, v8, s[16:17]
	v_cmp_le_u32_e64 s[16:17], s6, v165
	v_addc_co_u32_e64 v8, s[20:21], 0, v8, s[8:9]
	v_cmp_le_u32_e64 s[8:9], s6, v166
	v_addc_co_u32_e64 v8, s[20:21], 0, v8, s[12:13]
	v_addc_co_u32_e64 v8, s[20:21], 0, v8, s[16:17]
	v_addc_co_u32_e64 v8, s[20:21], 0, v8, s[8:9]
	v_and_b32_e32 v9, 16, v8
	v_cmp_ne_u32_e64 s[22:23], 0, v9
	v_and_b32_e32 v9, 8, v8
	v_cmp_ne_u32_e64 s[18:19], 0, v9
	v_and_b32_e32 v9, 4, v8
	v_cmp_ne_u32_e64 s[16:17], 0, v9
	v_and_b32_e32 v9, 2, v8
	v_cmp_ne_u32_e64 s[12:13], 0, v9
	v_and_b32_e32 v9, 1, v8
	v_cmp_ne_u32_e64 s[8:9], 0, v9
	s_bcnt1_i32_b64 s7, s[22:23]
	s_bcnt1_i32_b64 s3, s[18:19]
	s_lshl1_add_u32 s7, s7, s3
	s_bcnt1_i32_b64 s3, s[16:17]
	s_lshl1_add_u32 s7, s7, s3
	s_bcnt1_i32_b64 s3, s[12:13]
	s_lshl1_add_u32 s7, s7, s3
	s_bcnt1_i32_b64 s3, s[8:9]
	s_lshl1_add_u32 s7, s7, s3
	s_cmpk_lt_u32 s7, 0x100
	s_cselect_b32 s4, s4, s6
	s_cmpk_eq_u32 s7, 0x100
	s_cbranch_scc1 .Ltk2_x28
	s_lshr_b32 s5, s5, 1
	s_cbranch_scc1 .Ltk2_l28
	s_branch .Ltk2_orig

.Ltk2_l20:
	s_or_b32 s6, s4, s5
	v_cmp_le_u32_e64 s[8:9], s6, v111
	v_cmp_le_u32_e64 s[12:13], s6, v113
	v_cmp_le_u32_e64 s[16:17], s6, v115
	v_cndmask_b32_e64 v8, 0, 1, s[8:9]
	v_cmp_le_u32_e64 s[8:9], s6, v117
	v_addc_co_u32_e64 v8, s[20:21], 0, v8, s[12:13]
	v_cmp_le_u32_e64 s[12:13], s6, v119
	v_addc_co_u32_e64 v8, s[20:21], 0, v8, s[16:17]
	v_cmp_le_u32_e64 s[16:17], s6, v121
	v_addc_co_u32_e64 v8, s[20:21], 0, v8, s[8:9]
	v_cmp_le_u32_e64 s[8:9], s6, v123
	v_addc_co_u32_e64 v8, s[20:21], 0, v8, s[12:13]
	v_cmp_le_u32_e64 s[12:13], s6, v124
	v_addc_co_u32_e64 v8, s[20:21], 0, v8, s[16:17]
	v_cmp_le_u32_e64 s[16:17], s6, v125
	v_addc_co_u32_e64 v8, s[20:21], 0, v8, s[8:9]
	v_cmp_le_u32_e64 s[8:9], s6, v126
	v_addc_co_u32_e64 v8, s[20:21], 0, v8, s[12:13]
	v_cmp_le_u32_e64 s[12:13], s6, v127
	v_addc_co_u32_e64 v8, s[20:21], 0, v8, s[16:17]
	v_cmp_le_u32_e64 s[16:17], s6, v128
	v_addc_co_u32_e64 v8, s[20:21], 0, v8, s[8:9]
	v_cmp_le_u32_e64 s[8:9], s6, v129
	v_addc_co_u32_e64 v8, s[20:21], 0, v8, s[12:13]
	v_cmp_le_u32_e64 s[12:13], s6, v130
	v_addc_co_u32_e64 v8, s[20:21], 0, v8, s[16:17]
	v_cmp_le_u32_e64 s[16:17], s6, v132
	v_addc_co_u32_e64 v8, s[20:21], 0, v8, s[8:9]
	v_cmp_le_u32_e64 s[8:9], s6, v133
	v_addc_co_u32_e64 v8, s[20:21], 0, v8, s[12:13]
	v_cmp_le_u32_e64 s[12:13], s6, v138
	v_addc_co_u32_e64 v8, s[20:21], 0, v8, s[16:17]
	v_cmp_le_u32_e64 s[16:17], s6, v139
	v_addc_co_u32_e64 v8, s[20:21], 0, v8, s[8:9]
	v_cmp_le_u32_e64 s[8:9], s6, v141
	v_addc_co_u32_e64 v8, s[20:21], 0, v8, s[12:13]
	v_cmp_le_u32_e64 s[12:13], s6, v143
	v_addc_co_u32_e64 v8, s[20:21], 0, v8, s[16:17]
	v_addc_co_u32_e64 v8, s[20:21], 0, v8, s[8:9]
	v_addc_co_u32_e64 v8, s[20:21], 0, v8, s[12:13]
	v_and_b32_e32 v9, 16, v8
	v_cmp_ne_u32_e64 s[22:23], 0, v9
	v_and_b32_e32 v9, 8, v8
	v_cmp_ne_u32_e64 s[18:19], 0, v9
	v_and_b32_e32 v9, 4, v8
	v_cmp_ne_u32_e64 s[16:17], 0, v9
	v_and_b32_e32 v9, 2, v8
	v_cmp_ne_u32_e64 s[12:13], 0, v9
	v_and_b32_e32 v9, 1, v8
	v_cmp_ne_u32_e64 s[8:9], 0, v9
	s_bcnt1_i32_b64 s7, s[22:23]
	s_bcnt1_i32_b64 s3, s[18:19]
	s_lshl1_add_u32 s7, s7, s3
	s_bcnt1_i32_b64 s3, s[16:17]
	s_lshl1_add_u32 s7, s7, s3
	s_bcnt1_i32_b64 s3, s[12:13]
	s_lshl1_add_u32 s7, s7, s3
	s_bcnt1_i32_b64 s3, s[8:9]
	s_lshl1_add_u32 s7, s7, s3
	s_cmpk_lt_u32 s7, 0x100
	s_cselect_b32 s4, s4, s6
	s_cmpk_eq_u32 s7, 0x100
	s_cbranch_scc1 .Ltk2_x20
	s_lshr_b32 s5, s5, 1
	s_cbranch_scc1 .Ltk2_l20
	s_branch .Ltk2_orig

.Ltk2_l12:
	s_or_b32 s6, s4, s5
	v_cmp_le_u32_e64 s[8:9], s6, v111
	v_cmp_le_u32_e64 s[12:13], s6, v113
	v_cmp_le_u32_e64 s[16:17], s6, v115
	v_cndmask_b32_e64 v8, 0, 1, s[8:9]
	v_cmp_le_u32_e64 s[8:9], s6, v117
	v_addc_co_u32_e64 v8, s[20:21], 0, v8, s[12:13]
	v_cmp_le_u32_e64 s[12:13], s6, v119
	v_addc_co_u32_e64 v8, s[20:21], 0, v8, s[16:17]
	v_cmp_le_u32_e64 s[16:17], s6, v121
	v_addc_co_u32_e64 v8, s[20:21], 0, v8, s[8:9]
	v_cmp_le_u32_e64 s[8:9], s6, v123
	v_addc_co_u32_e64 v8, s[20:21], 0, v8, s[12:13]
	v_cmp_le_u32_e64 s[12:13], s6, v124
	v_addc_co_u32_e64 v8, s[20:21], 0, v8, s[16:17]
	v_cmp_le_u32_e64 s[16:17], s6, v125
	v_addc_co_u32_e64 v8, s[20:21], 0, v8, s[8:9]
	v_cmp_le_u32_e64 s[8:9], s6, v126
	v_addc_co_u32_e64 v8, s[20:21], 0, v8, s[12:13]
	v_cmp_le_u32_e64 s[12:13], s6, v127
	v_addc_co_u32_e64 v8, s[20:21], 0, v8, s[16:17]
	v_cmp_le_u32_e64 s[16:17], s6, v128
	v_addc_co_u32_e64 v8, s[20:21], 0, v8, s[8:9]
	v_addc_co_u32_e64 v8, s[20:21], 0, v8, s[12:13]
	v_addc_co_u32_e64 v8, s[20:21], 0, v8, s[16:17]
	v_and_b32_e32 v9, 8, v8
	v_cmp_ne_u32_e64 s[18:19], 0, v9
	v_and_b32_e32 v9, 4, v8
	v_cmp_ne_u32_e64 s[16:17], 0, v9
	v_and_b32_e32 v9, 2, v8
	v_cmp_ne_u32_e64 s[12:13], 0, v9
	v_and_b32_e32 v9, 1, v8
	v_cmp_ne_u32_e64 s[8:9], 0, v9
	s_bcnt1_i32_b64 s7, s[18:19]
	s_bcnt1_i32_b64 s3, s[16:17]
	s_lshl1_add_u32 s7, s7, s3
	s_bcnt1_i32_b64 s3, s[12:13]
	s_lshl1_add_u32 s7, s7, s3
	s_bcnt1_i32_b64 s3, s[8:9]
	s_lshl1_add_u32 s7, s7, s3
	s_cmpk_lt_u32 s7, 0x100
	s_cselect_b32 s4, s4, s6
	s_cmpk_eq_u32 s7, 0x100
	s_cbranch_scc1 .Ltk2_x12
	s_lshr_b32 s5, s5, 1
	s_cbranch_scc1 .Ltk2_l12
	s_branch .Ltk2_orig

.Ltk2_x28:
	v_cmp_le_u32_e64 s[8:9], s4, v111
	v_cmp_le_u32_e64 s[12:13], s4, v113
	v_cmp_le_u32_e64 s[16:17], s4, v115
	s_nop 0
	v_writelane_b32 v10, s8, 0
	v_writelane_b32 v11, s9, 0
	v_cmp_le_u32_e64 s[8:9], s4, v117
	v_writelane_b32 v10, s12, 1
	v_writelane_b32 v11, s13, 1
	v_cmp_le_u32_e64 s[12:13], s4, v119
	v_writelane_b32 v10, s16, 2
	v_writelane_b32 v11, s17, 2
	v_cmp_le_u32_e64 s[16:17], s4, v121
	v_writelane_b32 v10, s8, 3
	v_writelane_b32 v11, s9, 3
	v_cmp_le_u32_e64 s[8:9], s4, v123
	v_writelane_b32 v10, s12, 4
	v_writelane_b32 v11, s13, 4
	v_cmp_le_u32_e64 s[12:13], s4, v124
	v_writelane_b32 v10, s16, 5
	v_writelane_b32 v11, s17, 5
	v_cmp_le_u32_e64 s[16:17], s4, v125
	v_writelane_b32 v10, s8, 6
	v_writelane_b32 v11, s9, 6
	v_cmp_le_u32_e64 s[8:9], s4, v126
	v_writelane_b32 v10, s12, 7
	v_writelane_b32 v11, s13, 7
	v_cmp_le_u32_e64 s[12:13], s4, v127
	v_writelane_b32 v10, s16, 8
	v_writelane_b32 v11, s17, 8
	v_cmp_le_u32_e64 s[16:17], s4, v128
	v_writelane_b32 v10, s8, 9
	v_writelane_b32 v11, s9, 9
	v_cmp_le_u32_e64 s[8:9], s4, v129
	v_writelane_b32 v10, s12, 10
	v_writelane_b32 v11, s13, 10
	v_cmp_le_u32_e64 s[12:13], s4, v130
	v_writelane_b32 v10, s16, 11
	v_writelane_b32 v11, s17, 11
	v_cmp_le_u32_e64 s[16:17], s4, v132
	v_writelane_b32 v10, s8, 12
	v_writelane_b32 v11, s9, 12
	v_cmp_le_u32_e64 s[8:9], s4, v133
	v_writelane_b32 v10, s12, 13
	v_writelane_b32 v11, s13, 13
	v_cmp_le_u32_e64 s[12:13], s4, v138
	v_writelane_b32 v10, s16, 14
	v_writelane_b32 v11, s17, 14
	v_cmp_le_u32_e64 s[16:17], s4, v139
	v_writelane_b32 v10, s8, 15
	v_writelane_b32 v11, s9, 15
	v_cmp_le_u32_e64 s[8:9], s4, v141
	v_writelane_b32 v10, s12, 16
	v_writelane_b32 v11, s13, 16
	v_cmp_le_u32_e64 s[12:13], s4, v143
	v_writelane_b32 v10, s16, 17
	v_writelane_b32 v11, s17, 17
	v_cmp_le_u32_e64 s[16:17], s4, v145
	v_writelane_b32 v10, s8, 18
	v_writelane_b32 v11, s9, 18
	v_cmp_le_u32_e64 s[8:9], s4, v147
	v_writelane_b32 v10, s12, 19
	v_writelane_b32 v11, s13, 19
	v_cmp_le_u32_e64 s[12:13], s4, v149
	v_writelane_b32 v10, s16, 20
	v_writelane_b32 v11, s17, 20
	v_cmp_le_u32_e64 s[16:17], s4, v151
	v_writelane_b32 v10, s8, 21
	v_writelane_b32 v11, s9, 21
	v_cmp_le_u32_e64 s[8:9], s4, v160
	v_writelane_b32 v10, s12, 22
	v_writelane_b32 v11, s13, 22
	v_cmp_le_u32_e64 s[12:13], s4, v163
	v_writelane_b32 v10, s16, 23
	v_writelane_b32 v11, s17, 23
	v_cmp_le_u32_e64 s[16:17], s4, v165
	v_writelane_b32 v10, s8, 24
	v_writelane_b32 v11, s9, 24
	v_cmp_le_u32_e64 s[8:9], s4, v166
	v_writelane_b32 v10, s12, 25
	v_writelane_b32 v11, s13, 25
	v_writelane_b32 v10, s16, 26
	v_writelane_b32 v11, s17, 26
	v_writelane_b32 v10, s8, 27
	v_writelane_b32 v11, s9, 27
	v_mov_b32_e32 v2, v10
	v_mov_b32_e32 v3, v11
	s_branch .LBB0_2415

.Ltk2_x20:
	v_cmp_le_u32_e64 s[8:9], s4, v111
	v_cmp_le_u32_e64 s[12:13], s4, v113
	v_cmp_le_u32_e64 s[16:17], s4, v115
	s_nop 0
	v_writelane_b32 v10, s8, 0
	v_writelane_b32 v11, s9, 0
	v_cmp_le_u32_e64 s[8:9], s4, v117
	v_writelane_b32 v10, s12, 1
	v_writelane_b32 v11, s13, 1
	v_cmp_le_u32_e64 s[12:13], s4, v119
	v_writelane_b32 v10, s16, 2
	v_writelane_b32 v11, s17, 2
	v_cmp_le_u32_e64 s[16:17], s4, v121
	v_writelane_b32 v10, s8, 3
	v_writelane_b32 v11, s9, 3
	v_cmp_le_u32_e64 s[8:9], s4, v123
	v_writelane_b32 v10, s12, 4
	v_writelane_b32 v11, s13, 4
	v_cmp_le_u32_e64 s[12:13], s4, v124
	v_writelane_b32 v10, s16, 5
	v_writelane_b32 v11, s17, 5
	v_cmp_le_u32_e64 s[16:17], s4, v125
	v_writelane_b32 v10, s8, 6
	v_writelane_b32 v11, s9, 6
	v_cmp_le_u32_e64 s[8:9], s4, v126
	v_writelane_b32 v10, s12, 7
	v_writelane_b32 v11, s13, 7
	v_cmp_le_u32_e64 s[12:13], s4, v127
	v_writelane_b32 v10, s16, 8
	v_writelane_b32 v11, s17, 8
	v_cmp_le_u32_e64 s[16:17], s4, v128
	v_writelane_b32 v10, s8, 9
	v_writelane_b32 v11, s9, 9
	v_cmp_le_u32_e64 s[8:9], s4, v129
	v_writelane_b32 v10, s12, 10
	v_writelane_b32 v11, s13, 10
	v_cmp_le_u32_e64 s[12:13], s4, v130
	v_writelane_b32 v10, s16, 11
	v_writelane_b32 v11, s17, 11
	v_cmp_le_u32_e64 s[16:17], s4, v132
	v_writelane_b32 v10, s8, 12
	v_writelane_b32 v11, s9, 12
	v_cmp_le_u32_e64 s[8:9], s4, v133
	v_writelane_b32 v10, s12, 13
	v_writelane_b32 v11, s13, 13
	v_cmp_le_u32_e64 s[12:13], s4, v138
	v_writelane_b32 v10, s16, 14
	v_writelane_b32 v11, s17, 14
	v_cmp_le_u32_e64 s[16:17], s4, v139
	v_writelane_b32 v10, s8, 15
	v_writelane_b32 v11, s9, 15
	v_cmp_le_u32_e64 s[8:9], s4, v141
	v_writelane_b32 v10, s12, 16
	v_writelane_b32 v11, s13, 16
	v_cmp_le_u32_e64 s[12:13], s4, v143
	v_writelane_b32 v10, s16, 17
	v_writelane_b32 v11, s17, 17
	v_writelane_b32 v10, s8, 18
	v_writelane_b32 v11, s9, 18
	v_writelane_b32 v10, s12, 19
	v_writelane_b32 v11, s13, 19
	v_mov_b32_e32 v2, v10
	v_mov_b32_e32 v3, v11
	s_branch .LBB0_2415

.Ltk2_x12:
	v_cmp_le_u32_e64 s[8:9], s4, v111
	v_cmp_le_u32_e64 s[12:13], s4, v113
	v_cmp_le_u32_e64 s[16:17], s4, v115
	s_nop 0
	v_writelane_b32 v10, s8, 0
	v_writelane_b32 v11, s9, 0
	v_cmp_le_u32_e64 s[8:9], s4, v117
	v_writelane_b32 v10, s12, 1
	v_writelane_b32 v11, s13, 1
	v_cmp_le_u32_e64 s[12:13], s4, v119
	v_writelane_b32 v10, s16, 2
	v_writelane_b32 v11, s17, 2
	v_cmp_le_u32_e64 s[16:17], s4, v121
	v_writelane_b32 v10, s8, 3
	v_writelane_b32 v11, s9, 3
	v_cmp_le_u32_e64 s[8:9], s4, v123
	v_writelane_b32 v10, s12, 4
	v_writelane_b32 v11, s13, 4
	v_cmp_le_u32_e64 s[12:13], s4, v124
	v_writelane_b32 v10, s16, 5
	v_writelane_b32 v11, s17, 5
	v_cmp_le_u32_e64 s[16:17], s4, v125
	v_writelane_b32 v10, s8, 6
	v_writelane_b32 v11, s9, 6
	v_cmp_le_u32_e64 s[8:9], s4, v126
	v_writelane_b32 v10, s12, 7
	v_writelane_b32 v11, s13, 7
	v_cmp_le_u32_e64 s[12:13], s4, v127
	v_writelane_b32 v10, s16, 8
	v_writelane_b32 v11, s17, 8
	v_cmp_le_u32_e64 s[16:17], s4, v128
	v_writelane_b32 v10, s8, 9
	v_writelane_b32 v11, s9, 9
	v_writelane_b32 v10, s12, 10
	v_writelane_b32 v11, s13, 10
	v_writelane_b32 v10, s16, 11
	v_writelane_b32 v11, s17, 11
	v_mov_b32_e32 v2, v10
	v_mov_b32_e32 v3, v11
	s_branch .LBB0_2415

.Ltk3_l28:
	s_or_b32 s6, s4, s5
	v_cmp_le_u32_e64 s[8:9], s6, v93
	v_cmp_le_u32_e64 s[12:13], s6, v94
	v_cmp_le_u32_e64 s[16:17], s6, v95
	v_cndmask_b32_e64 v8, 0, 1, s[8:9]
	v_cmp_le_u32_e64 s[8:9], s6, v96
	v_addc_co_u32_e64 v8, s[20:21], 0, v8, s[12:13]
	v_cmp_le_u32_e64 s[12:13], s6, v97
	v_addc_co_u32_e64 v8, s[20:21], 0, v8, s[16:17]
	v_cmp_le_u32_e64 s[16:17], s6, v98
	v_addc_co_u32_e64 v8, s[20:21], 0, v8, s[8:9]
	v_cmp_le_u32_e64 s[8:9], s6, v99
	v_addc_co_u32_e64 v8, s[20:21], 0, v8, s[12:13]
	v_cmp_le_u32_e64 s[12:13], s6, v100
	v_addc_co_u32_e64 v8, s[20:21], 0, v8, s[16:17]
	v_cmp_le_u32_e64 s[16:17], s6, v101
	v_addc_co_u32_e64 v8, s[20:21], 0, v8, s[8:9]
	v_cmp_le_u32_e64 s[8:9], s6, v102
	v_addc_co_u32_e64 v8, s[20:21], 0, v8, s[12:13]
	v_cmp_le_u32_e64 s[12:13], s6, v103
	v_addc_co_u32_e64 v8, s[20:21], 0, v8, s[16:17]
	v_cmp_le_u32_e64 s[16:17], s6, v104
	v_addc_co_u32_e64 v8, s[20:21], 0, v8, s[8:9]
	v_cmp_le_u32_e64 s[8:9], s6, v105
	v_addc_co_u32_e64 v8, s[20:21], 0, v8, s[12:13]
	v_cmp_le_u32_e64 s[12:13], s6, v106
	v_addc_co_u32_e64 v8, s[20:21], 0, v8, s[16:17]
	v_cmp_le_u32_e64 s[16:17], s6, v107
	v_addc_co_u32_e64 v8, s[20:21], 0, v8, s[8:9]
	v_cmp_le_u32_e64 s[8:9], s6, v108
	v_addc_co_u32_e64 v8, s[20:21], 0, v8, s[12:13]
	v_cmp_le_u32_e64 s[12:13], s6, v109
	v_addc_co_u32_e64 v8, s[20:21], 0, v8, s[16:17]
	v_cmp_le_u32_e64 s[16:17], s6, v110
	v_addc_co_u32_e64 v8, s[20:21], 0, v8, s[8:9]
	v_cmp_le_u32_e64 s[8:9], s6, v112
	v_addc_co_u32_e64 v8, s[20:21], 0, v8, s[12:13]
	v_cmp_le_u32_e64 s[12:13], s6, v114
	v_addc_co_u32_e64 v8, s[20:21], 0, v8, s[16:17]
	v_cmp_le_u32_e64 s[16:17], s6, v116
	v_addc_co_u32_e64 v8, s[20:21], 0, v8, s[8:9]
	v_cmp_le_u32_e64 s[8:9], s6, v118
	v_addc_co_u32_e64 v8, s[20:21], 0, v8, s[12:13]
	v_cmp_le_u32_e64 s[12:13], s6, v120
	v_addc_co_u32_e64 v8, s[20:21], 0, v8, s[16:17]
	v_cmp_le_u32_e64 s[16:17], s6, v122
	v_addc_co_u32_e64 v8, s[20:21], 0, v8, s[8:9]
	v_cmp_le_u32_e64 s[8:9], s6, v131
	v_addc_co_u32_e64 v8, s[20:21], 0, v8, s[12:13]
	v_cmp_le_u32_e64 s[12:13], s6, v90
	v_addc_co_u32_e64 v8, s[20:21], 0, v8, s[16:17]
	v_cmp_le_u32_e64 s[16:17], s6, v91
	v_addc_co_u32_e64 v8, s[20:21], 0, v8, s[8:9]
	v_cmp_le_u32_e64 s[8:9], s6, v134
	v_addc_co_u32_e64 v8, s[20:21], 0, v8, s[12:13]
	v_addc_co_u32_e64 v8, s[20:21], 0, v8, s[16:17]
	v_addc_co_u32_e64 v8, s[20:21], 0, v8, s[8:9]
	v_and_b32_e32 v9, 16, v8
	v_cmp_ne_u32_e64 s[22:23], 0, v9
	v_and_b32_e32 v9, 8, v8
	v_cmp_ne_u32_e64 s[18:19], 0, v9
	v_and_b32_e32 v9, 4, v8
	v_cmp_ne_u32_e64 s[16:17], 0, v9
	v_and_b32_e32 v9, 2, v8
	v_cmp_ne_u32_e64 s[12:13], 0, v9
	v_and_b32_e32 v9, 1, v8
	v_cmp_ne_u32_e64 s[8:9], 0, v9
	s_bcnt1_i32_b64 s7, s[22:23]
	s_bcnt1_i32_b64 s3, s[18:19]
	s_lshl1_add_u32 s7, s7, s3
	s_bcnt1_i32_b64 s3, s[16:17]
	s_lshl1_add_u32 s7, s7, s3
	s_bcnt1_i32_b64 s3, s[12:13]
	s_lshl1_add_u32 s7, s7, s3
	s_bcnt1_i32_b64 s3, s[8:9]
	s_lshl1_add_u32 s7, s7, s3
	s_cmpk_lt_u32 s7, 0x100
	s_cselect_b32 s4, s4, s6
	s_cmpk_eq_u32 s7, 0x100
	s_cbranch_scc1 .Ltk3_x28
	s_lshr_b32 s5, s5, 1
	s_cbranch_scc1 .Ltk3_l28
	s_branch .Ltk3_orig

.Ltk3_l20:
	s_or_b32 s6, s4, s5
	v_cmp_le_u32_e64 s[8:9], s6, v93
	v_cmp_le_u32_e64 s[12:13], s6, v94
	v_cmp_le_u32_e64 s[16:17], s6, v95
	v_cndmask_b32_e64 v8, 0, 1, s[8:9]
	v_cmp_le_u32_e64 s[8:9], s6, v96
	v_addc_co_u32_e64 v8, s[20:21], 0, v8, s[12:13]
	v_cmp_le_u32_e64 s[12:13], s6, v97
	v_addc_co_u32_e64 v8, s[20:21], 0, v8, s[16:17]
	v_cmp_le_u32_e64 s[16:17], s6, v98
	v_addc_co_u32_e64 v8, s[20:21], 0, v8, s[8:9]
	v_cmp_le_u32_e64 s[8:9], s6, v99
	v_addc_co_u32_e64 v8, s[20:21], 0, v8, s[12:13]
	v_cmp_le_u32_e64 s[12:13], s6, v100
	v_addc_co_u32_e64 v8, s[20:21], 0, v8, s[16:17]
	v_cmp_le_u32_e64 s[16:17], s6, v101
	v_addc_co_u32_e64 v8, s[20:21], 0, v8, s[8:9]
	v_cmp_le_u32_e64 s[8:9], s6, v102
	v_addc_co_u32_e64 v8, s[20:21], 0, v8, s[12:13]
	v_cmp_le_u32_e64 s[12:13], s6, v103
	v_addc_co_u32_e64 v8, s[20:21], 0, v8, s[16:17]
	v_cmp_le_u32_e64 s[16:17], s6, v104
	v_addc_co_u32_e64 v8, s[20:21], 0, v8, s[8:9]
	v_cmp_le_u32_e64 s[8:9], s6, v105
	v_addc_co_u32_e64 v8, s[20:21], 0, v8, s[12:13]
	v_cmp_le_u32_e64 s[12:13], s6, v106
	v_addc_co_u32_e64 v8, s[20:21], 0, v8, s[16:17]
	v_cmp_le_u32_e64 s[16:17], s6, v107
	v_addc_co_u32_e64 v8, s[20:21], 0, v8, s[8:9]
	v_cmp_le_u32_e64 s[8:9], s6, v108
	v_addc_co_u32_e64 v8, s[20:21], 0, v8, s[12:13]
	v_cmp_le_u32_e64 s[12:13], s6, v109
	v_addc_co_u32_e64 v8, s[20:21], 0, v8, s[16:17]
	v_cmp_le_u32_e64 s[16:17], s6, v110
	v_addc_co_u32_e64 v8, s[20:21], 0, v8, s[8:9]
	v_cmp_le_u32_e64 s[8:9], s6, v112
	v_addc_co_u32_e64 v8, s[20:21], 0, v8, s[12:13]
	v_cmp_le_u32_e64 s[12:13], s6, v114
	v_addc_co_u32_e64 v8, s[20:21], 0, v8, s[16:17]
	v_addc_co_u32_e64 v8, s[20:21], 0, v8, s[8:9]
	v_addc_co_u32_e64 v8, s[20:21], 0, v8, s[12:13]
	v_and_b32_e32 v9, 16, v8
	v_cmp_ne_u32_e64 s[22:23], 0, v9
	v_and_b32_e32 v9, 8, v8
	v_cmp_ne_u32_e64 s[18:19], 0, v9
	v_and_b32_e32 v9, 4, v8
	v_cmp_ne_u32_e64 s[16:17], 0, v9
	v_and_b32_e32 v9, 2, v8
	v_cmp_ne_u32_e64 s[12:13], 0, v9
	v_and_b32_e32 v9, 1, v8
	v_cmp_ne_u32_e64 s[8:9], 0, v9
	s_bcnt1_i32_b64 s7, s[22:23]
	s_bcnt1_i32_b64 s3, s[18:19]
	s_lshl1_add_u32 s7, s7, s3
	s_bcnt1_i32_b64 s3, s[16:17]
	s_lshl1_add_u32 s7, s7, s3
	s_bcnt1_i32_b64 s3, s[12:13]
	s_lshl1_add_u32 s7, s7, s3
	s_bcnt1_i32_b64 s3, s[8:9]
	s_lshl1_add_u32 s7, s7, s3
	s_cmpk_lt_u32 s7, 0x100
	s_cselect_b32 s4, s4, s6
	s_cmpk_eq_u32 s7, 0x100
	s_cbranch_scc1 .Ltk3_x20
	s_lshr_b32 s5, s5, 1
	s_cbranch_scc1 .Ltk3_l20
	s_branch .Ltk3_orig

.Ltk3_l12:
	s_or_b32 s6, s4, s5
	v_cmp_le_u32_e64 s[8:9], s6, v93
	v_cmp_le_u32_e64 s[12:13], s6, v94
	v_cmp_le_u32_e64 s[16:17], s6, v95
	v_cndmask_b32_e64 v8, 0, 1, s[8:9]
	v_cmp_le_u32_e64 s[8:9], s6, v96
	v_addc_co_u32_e64 v8, s[20:21], 0, v8, s[12:13]
	v_cmp_le_u32_e64 s[12:13], s6, v97
	v_addc_co_u32_e64 v8, s[20:21], 0, v8, s[16:17]
	v_cmp_le_u32_e64 s[16:17], s6, v98
	v_addc_co_u32_e64 v8, s[20:21], 0, v8, s[8:9]
	v_cmp_le_u32_e64 s[8:9], s6, v99
	v_addc_co_u32_e64 v8, s[20:21], 0, v8, s[12:13]
	v_cmp_le_u32_e64 s[12:13], s6, v100
	v_addc_co_u32_e64 v8, s[20:21], 0, v8, s[16:17]
	v_cmp_le_u32_e64 s[16:17], s6, v101
	v_addc_co_u32_e64 v8, s[20:21], 0, v8, s[8:9]
	v_cmp_le_u32_e64 s[8:9], s6, v102
	v_addc_co_u32_e64 v8, s[20:21], 0, v8, s[12:13]
	v_cmp_le_u32_e64 s[12:13], s6, v103
	v_addc_co_u32_e64 v8, s[20:21], 0, v8, s[16:17]
	v_cmp_le_u32_e64 s[16:17], s6, v104
	v_addc_co_u32_e64 v8, s[20:21], 0, v8, s[8:9]
	v_addc_co_u32_e64 v8, s[20:21], 0, v8, s[12:13]
	v_addc_co_u32_e64 v8, s[20:21], 0, v8, s[16:17]
	v_and_b32_e32 v9, 8, v8
	v_cmp_ne_u32_e64 s[18:19], 0, v9
	v_and_b32_e32 v9, 4, v8
	v_cmp_ne_u32_e64 s[16:17], 0, v9
	v_and_b32_e32 v9, 2, v8
	v_cmp_ne_u32_e64 s[12:13], 0, v9
	v_and_b32_e32 v9, 1, v8
	v_cmp_ne_u32_e64 s[8:9], 0, v9
	s_bcnt1_i32_b64 s7, s[18:19]
	s_bcnt1_i32_b64 s3, s[16:17]
	s_lshl1_add_u32 s7, s7, s3
	s_bcnt1_i32_b64 s3, s[12:13]
	s_lshl1_add_u32 s7, s7, s3
	s_bcnt1_i32_b64 s3, s[8:9]
	s_lshl1_add_u32 s7, s7, s3
	s_cmpk_lt_u32 s7, 0x100
	s_cselect_b32 s4, s4, s6
	s_cmpk_eq_u32 s7, 0x100
	s_cbranch_scc1 .Ltk3_x12
	s_lshr_b32 s5, s5, 1
	s_cbranch_scc1 .Ltk3_l12
	s_branch .Ltk3_orig

.Ltk3_x28:
	v_cmp_le_u32_e64 s[8:9], s4, v93
	v_cmp_le_u32_e64 s[12:13], s4, v94
	v_cmp_le_u32_e64 s[16:17], s4, v95
	s_nop 0
	v_writelane_b32 v10, s8, 0
	v_writelane_b32 v11, s9, 0
	v_cmp_le_u32_e64 s[8:9], s4, v96
	v_writelane_b32 v10, s12, 1
	v_writelane_b32 v11, s13, 1
	v_cmp_le_u32_e64 s[12:13], s4, v97
	v_writelane_b32 v10, s16, 2
	v_writelane_b32 v11, s17, 2
	v_cmp_le_u32_e64 s[16:17], s4, v98
	v_writelane_b32 v10, s8, 3
	v_writelane_b32 v11, s9, 3
	v_cmp_le_u32_e64 s[8:9], s4, v99
	v_writelane_b32 v10, s12, 4
	v_writelane_b32 v11, s13, 4
	v_cmp_le_u32_e64 s[12:13], s4, v100
	v_writelane_b32 v10, s16, 5
	v_writelane_b32 v11, s17, 5
	v_cmp_le_u32_e64 s[16:17], s4, v101
	v_writelane_b32 v10, s8, 6
	v_writelane_b32 v11, s9, 6
	v_cmp_le_u32_e64 s[8:9], s4, v102
	v_writelane_b32 v10, s12, 7
	v_writelane_b32 v11, s13, 7
	v_cmp_le_u32_e64 s[12:13], s4, v103
	v_writelane_b32 v10, s16, 8
	v_writelane_b32 v11, s17, 8
	v_cmp_le_u32_e64 s[16:17], s4, v104
	v_writelane_b32 v10, s8, 9
	v_writelane_b32 v11, s9, 9
	v_cmp_le_u32_e64 s[8:9], s4, v105
	v_writelane_b32 v10, s12, 10
	v_writelane_b32 v11, s13, 10
	v_cmp_le_u32_e64 s[12:13], s4, v106
	v_writelane_b32 v10, s16, 11
	v_writelane_b32 v11, s17, 11
	v_cmp_le_u32_e64 s[16:17], s4, v107
	v_writelane_b32 v10, s8, 12
	v_writelane_b32 v11, s9, 12
	v_cmp_le_u32_e64 s[8:9], s4, v108
	v_writelane_b32 v10, s12, 13
	v_writelane_b32 v11, s13, 13
	v_cmp_le_u32_e64 s[12:13], s4, v109
	v_writelane_b32 v10, s16, 14
	v_writelane_b32 v11, s17, 14
	v_cmp_le_u32_e64 s[16:17], s4, v110
	v_writelane_b32 v10, s8, 15
	v_writelane_b32 v11, s9, 15
	v_cmp_le_u32_e64 s[8:9], s4, v112
	v_writelane_b32 v10, s12, 16
	v_writelane_b32 v11, s13, 16
	v_cmp_le_u32_e64 s[12:13], s4, v114
	v_writelane_b32 v10, s16, 17
	v_writelane_b32 v11, s17, 17
	v_cmp_le_u32_e64 s[16:17], s4, v116
	v_writelane_b32 v10, s8, 18
	v_writelane_b32 v11, s9, 18
	v_cmp_le_u32_e64 s[8:9], s4, v118
	v_writelane_b32 v10, s12, 19
	v_writelane_b32 v11, s13, 19
	v_cmp_le_u32_e64 s[12:13], s4, v120
	v_writelane_b32 v10, s16, 20
	v_writelane_b32 v11, s17, 20
	v_cmp_le_u32_e64 s[16:17], s4, v122
	v_writelane_b32 v10, s8, 21
	v_writelane_b32 v11, s9, 21
	v_cmp_le_u32_e64 s[8:9], s4, v131
	v_writelane_b32 v10, s12, 22
	v_writelane_b32 v11, s13, 22
	v_cmp_le_u32_e64 s[12:13], s4, v90
	v_writelane_b32 v10, s16, 23
	v_writelane_b32 v11, s17, 23
	v_cmp_le_u32_e64 s[16:17], s4, v91
	v_writelane_b32 v10, s8, 24
	v_writelane_b32 v11, s9, 24
	v_cmp_le_u32_e64 s[8:9], s4, v134
	v_writelane_b32 v10, s12, 25
	v_writelane_b32 v11, s13, 25
	v_writelane_b32 v10, s16, 26
	v_writelane_b32 v11, s17, 26
	v_writelane_b32 v10, s8, 27
	v_writelane_b32 v11, s9, 27
	v_mov_b32_e32 v2, v10
	v_mov_b32_e32 v3, v11
	s_branch .LBB0_2681

.Ltk3_x20:
	v_cmp_le_u32_e64 s[8:9], s4, v93
	v_cmp_le_u32_e64 s[12:13], s4, v94
	v_cmp_le_u32_e64 s[16:17], s4, v95
	s_nop 0
	v_writelane_b32 v10, s8, 0
	v_writelane_b32 v11, s9, 0
	v_cmp_le_u32_e64 s[8:9], s4, v96
	v_writelane_b32 v10, s12, 1
	v_writelane_b32 v11, s13, 1
	v_cmp_le_u32_e64 s[12:13], s4, v97
	v_writelane_b32 v10, s16, 2
	v_writelane_b32 v11, s17, 2
	v_cmp_le_u32_e64 s[16:17], s4, v98
	v_writelane_b32 v10, s8, 3
	v_writelane_b32 v11, s9, 3
	v_cmp_le_u32_e64 s[8:9], s4, v99
	v_writelane_b32 v10, s12, 4
	v_writelane_b32 v11, s13, 4
	v_cmp_le_u32_e64 s[12:13], s4, v100
	v_writelane_b32 v10, s16, 5
	v_writelane_b32 v11, s17, 5
	v_cmp_le_u32_e64 s[16:17], s4, v101
	v_writelane_b32 v10, s8, 6
	v_writelane_b32 v11, s9, 6
	v_cmp_le_u32_e64 s[8:9], s4, v102
	v_writelane_b32 v10, s12, 7
	v_writelane_b32 v11, s13, 7
	v_cmp_le_u32_e64 s[12:13], s4, v103
	v_writelane_b32 v10, s16, 8
	v_writelane_b32 v11, s17, 8
	v_cmp_le_u32_e64 s[16:17], s4, v104
	v_writelane_b32 v10, s8, 9
	v_writelane_b32 v11, s9, 9
	v_cmp_le_u32_e64 s[8:9], s4, v105
	v_writelane_b32 v10, s12, 10
	v_writelane_b32 v11, s13, 10
	v_cmp_le_u32_e64 s[12:13], s4, v106
	v_writelane_b32 v10, s16, 11
	v_writelane_b32 v11, s17, 11
	v_cmp_le_u32_e64 s[16:17], s4, v107
	v_writelane_b32 v10, s8, 12
	v_writelane_b32 v11, s9, 12
	v_cmp_le_u32_e64 s[8:9], s4, v108
	v_writelane_b32 v10, s12, 13
	v_writelane_b32 v11, s13, 13
	v_cmp_le_u32_e64 s[12:13], s4, v109
	v_writelane_b32 v10, s16, 14
	v_writelane_b32 v11, s17, 14
	v_cmp_le_u32_e64 s[16:17], s4, v110
	v_writelane_b32 v10, s8, 15
	v_writelane_b32 v11, s9, 15
	v_cmp_le_u32_e64 s[8:9], s4, v112
	v_writelane_b32 v10, s12, 16
	v_writelane_b32 v11, s13, 16
	v_cmp_le_u32_e64 s[12:13], s4, v114
	v_writelane_b32 v10, s16, 17
	v_writelane_b32 v11, s17, 17
	v_writelane_b32 v10, s8, 18
	v_writelane_b32 v11, s9, 18
	v_writelane_b32 v10, s12, 19
	v_writelane_b32 v11, s13, 19
	v_mov_b32_e32 v2, v10
	v_mov_b32_e32 v3, v11
	s_branch .LBB0_2681

.Ltk3_x12:
	v_cmp_le_u32_e64 s[8:9], s4, v93
	v_cmp_le_u32_e64 s[12:13], s4, v94
	v_cmp_le_u32_e64 s[16:17], s4, v95
	s_nop 0
	v_writelane_b32 v10, s8, 0
	v_writelane_b32 v11, s9, 0
	v_cmp_le_u32_e64 s[8:9], s4, v96
	v_writelane_b32 v10, s12, 1
	v_writelane_b32 v11, s13, 1
	v_cmp_le_u32_e64 s[12:13], s4, v97
	v_writelane_b32 v10, s16, 2
	v_writelane_b32 v11, s17, 2
	v_cmp_le_u32_e64 s[16:17], s4, v98
	v_writelane_b32 v10, s8, 3
	v_writelane_b32 v11, s9, 3
	v_cmp_le_u32_e64 s[8:9], s4, v99
	v_writelane_b32 v10, s12, 4
	v_writelane_b32 v11, s13, 4
	v_cmp_le_u32_e64 s[12:13], s4, v100
	v_writelane_b32 v10, s16, 5
	v_writelane_b32 v11, s17, 5
	v_cmp_le_u32_e64 s[16:17], s4, v101
	v_writelane_b32 v10, s8, 6
	v_writelane_b32 v11, s9, 6
	v_cmp_le_u32_e64 s[8:9], s4, v102
	v_writelane_b32 v10, s12, 7
	v_writelane_b32 v11, s13, 7
	v_cmp_le_u32_e64 s[12:13], s4, v103
	v_writelane_b32 v10, s16, 8
	v_writelane_b32 v11, s17, 8
	v_cmp_le_u32_e64 s[16:17], s4, v104
	v_writelane_b32 v10, s8, 9
	v_writelane_b32 v11, s9, 9
	v_writelane_b32 v10, s12, 10
	v_writelane_b32 v11, s13, 10
	v_writelane_b32 v10, s16, 11
	v_writelane_b32 v11, s17, 11
	v_mov_b32_e32 v2, v10
	v_mov_b32_e32 v3, v11
	s_branch .LBB0_2681
